# attention: packed f32 row sum and O scaling, in-loop DMA addresses from per-lane constants set up once per role (about 90 fewer issue slots per unit)
# speedup vs baseline: 1.0083x; 1.0083x over previous
.LBB0_429:
	v_writelane_b32 v254, s78, 15
	s_add_u32 s1, s6, 0x1400000
	s_mov_b32 s2, s90
	v_writelane_b32 v254, s79, 16
	v_writelane_b32 v254, s1, 17
	s_addc_u32 s1, s7, 0
	v_writelane_b32 v254, s1, 18
	v_lshlrev_b32_e32 v10, 1, v4
	v_writelane_b32 v254, s2, 19
	v_and_b32_e32 v10, 32, v10
	v_lshlrev_b32_e32 v11, 3, v4
	v_writelane_b32 v254, s3, 20
	s_add_i32 s1, s3, 32
	v_mov_b32_e32 v179, 0
	v_and_or_b32 v13, v11, 24, v10
	v_lshlrev_b32_e32 v10, 4, v4
	v_writelane_b32 v254, s1, 21
	s_or_b32 s1, s21, 0xffffff80
	v_and_b32_e32 v10, 0x70, v10
	v_mov_b32_e32 v11, v179
	v_writelane_b32 v254, s1, 22
	v_or_b32_e32 v192, s1, v5
	s_add_i32 s1, s3, 0xffffffa0
	v_lshl_add_u64 v[10:11], s[6:7], 0, v[10:11]
	s_mov_b64 s[4:5], 0x12000000
	v_writelane_b32 v254, s1, 23
	v_lshl_add_u64 v[184:185], v[10:11], 0, s[4:5]
	s_or_b32 s4, s3, 8
	v_writelane_b32 v254, s4, 24
	s_or_b32 s4, s3, 16
	v_writelane_b32 v254, s4, 25
	s_or_b32 s4, s3, 24
	v_writelane_b32 v254, s4, 26
	s_add_i32 s4, s3, 40
	v_writelane_b32 v254, s4, 27
	s_add_i32 s4, s3, 48
	v_writelane_b32 v254, s4, 28
	s_add_i32 s4, s3, 56
	v_writelane_b32 v254, s4, 29
	s_or_b32 s4, s21, 0xffffff88
	v_writelane_b32 v254, s4, 30
	s_or_b32 s4, s21, 0xffffff90
	v_writelane_b32 v254, s4, 31
	s_or_b32 s4, s21, 0xffffff98
	v_writelane_b32 v254, s4, 32
	s_add_i32 s4, s3, 0xffffffa8
	v_writelane_b32 v254, s4, 33
	s_add_i32 s4, s3, 0xffffffb0
	v_lshlrev_b32_e32 v12, 2, v6
	v_writelane_b32 v254, s4, 34
	s_add_i32 s4, s3, 0xffffffb8
	v_writelane_b32 v254, s4, 35
	v_cmp_gt_u32_e64 s[4:5], v12, v7
	v_or_b32_e32 v15, 1, v12
	v_cmp_lt_u32_e64 s[8:9], v12, v7
	v_writelane_b32 v254, s4, 36
	v_and_b32_e32 v3, 7, v4
	v_lshlrev_b32_e32 v193, 4, v3
	v_writelane_b32 v254, s5, 37
	v_cmp_lt_u32_e64 s[4:5], v15, v7
	v_or_b32_e32 v15, 2, v12
	v_lshlrev_b32_e32 v2, 3, v6
	v_writelane_b32 v254, s4, 38
	v_cmp_gt_u32_e64 s[6:7], 32, v8
	v_bitop3_b32 v8, v6, v4, 7 bitop3:0x78
	v_writelane_b32 v254, s5, 39
	v_cmp_lt_u32_e64 s[4:5], v15, v7
	v_bitop3_b32 v10, v6, v3, 2 bitop3:0x36
	v_bitop3_b32 v11, v6, v3, 4 bitop3:0x36
	v_writelane_b32 v254, s4, 40
	v_bitop3_b32 v3, v6, v3, 6 bitop3:0x36
	s_add_i32 s83, s75, 0x1000
	v_writelane_b32 v254, s5, 41
	v_cmp_gt_u32_e64 s[4:5], v15, v7
	v_or_b32_e32 v15, 3, v12
	v_or_b32_e32 v1, s3, v7
	v_writelane_b32 v254, s4, 42
	v_bitop3_b32 v9, v5, v4, 7 bitop3:0x78
	v_lshl_add_u32 v14, v7, 7, s75
	v_writelane_b32 v254, s5, 43
	v_cmp_lt_u32_e64 s[4:5], v15, v7
	v_or_b32_e32 v19, 8, v5
	s_lshl_b32 s22, s90, 2
	v_writelane_b32 v254, s4, 44
	v_lshl_add_u32 v18, v5, 7, s75
	v_or_b32_e32 v203, s3, v5
	v_writelane_b32 v254, s5, 45
	v_cmp_gt_u32_e64 s[4:5], v15, v7
	v_or_b32_e32 v15, 8, v12
	v_lshl_add_u32 v20, v19, 7, s75
	v_writelane_b32 v254, s4, 46
	v_or_b32_e32 v204, s3, v19
	v_or_b32_e32 v19, 16, v5
	v_writelane_b32 v254, s5, 47
	v_cmp_lt_u32_e64 s[4:5], v15, v7
	v_add_u32_e32 v194, v14, v2
	v_lshlrev_b32_e32 v8, 4, v8
	v_writelane_b32 v254, s4, 48
	v_lshlrev_b32_e32 v10, 4, v10
	v_lshlrev_b32_e32 v11, 4, v11
	v_writelane_b32 v254, s5, 49
	v_cmp_gt_u32_e64 s[4:5], v15, v7
	v_or_b32_e32 v15, 9, v12
	v_lshlrev_b32_e32 v3, 4, v3
	v_writelane_b32 v254, s4, 50
	v_xor_b32_e32 v16, 0x60, v193
	v_xor_b32_e32 v17, 0x70, v193
	v_writelane_b32 v254, s5, 51
	v_cmp_lt_u32_e64 s[4:5], v15, v7
	v_lshl_add_u32 v21, v19, 7, s75
	v_or_b32_e32 v205, s3, v19
	v_writelane_b32 v254, s4, 52
	v_lshlrev_b32_e32 v186, 1, v2
	v_mbcnt_lo_u32_b32 v2, -1, 0
	v_writelane_b32 v254, s5, 53
	v_cmp_gt_u32_e64 s[4:5], v15, v7
	v_or_b32_e32 v15, 10, v12
	s_xor_b32 s1, s3, 0x7f
	v_writelane_b32 v254, s4, 54
	s_add_i32 s2, s3, 64
	s_add_i32 s10, s3, 0x48
	v_writelane_b32 v254, s5, 55
	v_cmp_lt_u32_e64 s[4:5], v15, v7
	s_add_i32 s11, s3, 0x50
	s_add_i32 s12, s3, 0x58
	v_writelane_b32 v254, s4, 56
	s_add_i32 s13, s3, 0x60
	s_add_i32 s14, s3, 0x68
	v_writelane_b32 v254, s5, 57
	v_cmp_gt_u32_e64 s[4:5], v15, v7
	v_or_b32_e32 v15, 11, v12
	s_add_i32 s15, s3, 0x70
	v_writelane_b32 v254, s4, 58
	s_add_i32 s16, s3, 0x78
	s_or_b32 s17, s3, 0x80
	v_writelane_b32 v254, s5, 59
	v_cmp_lt_u32_e64 s[4:5], v15, v7
	s_or_b32 s18, s3, 0x88
	s_or_b32 s19, s3, 0x90
	v_writelane_b32 v254, s4, 60
	s_or_b32 s20, s3, 0x98
	v_or_b32_e32 v208, 0x1000, v193
	v_writelane_b32 v254, s5, 61
	v_cmp_gt_u32_e64 s[4:5], v15, v7
	v_or_b32_e32 v15, 16, v12
	s_mov_b32 s91, 0
	v_writelane_b32 v254, s4, 62
	s_movk_i32 s21, 0x1880
	s_mov_b64 s[92:93], 0x800
	v_writelane_b32 v254, s5, 63
	v_cmp_lt_u32_e64 s[4:5], v15, v7
	s_add_i32 s23, s75, 0x2400
	s_add_i32 s24, s75, 0x1000
	v_writelane_b32 v255, s4, 0
	s_add_i32 s25, s75, 0x2c00
	s_mov_b64 s[94:95], 0x1000
	v_writelane_b32 v255, s5, 1
	v_cmp_gt_u32_e64 s[4:5], v15, v7
	v_or_b32_e32 v15, 17, v12
	s_cmp_eq_u32 s3, 0
	s_cselect_b32 s26, 0, 0x4000
	s_add_i32 s26, s26, s75
	v_writelane_b32 v255, s4, 2
	s_add_i32 s27, s75, 0xc00
	s_add_i32 s28, s75, 0x1400
	v_writelane_b32 v255, s5, 3
	v_cmp_lt_u32_e64 s[4:5], v15, v7
	s_add_i32 s29, s75, 0x1800
	s_add_i32 s30, s75, 0x1c00
	v_writelane_b32 v255, s4, 4
	s_add_i32 s31, s75, 0x3000
	s_add_i32 s34, s75, 0x3400
	v_writelane_b32 v255, s5, 5
	v_cmp_gt_u32_e64 s[4:5], v15, v7
	v_or_b32_e32 v15, 18, v12
	s_add_i32 s35, s75, 0x3800
	v_writelane_b32 v255, s4, 6
	s_add_i32 s36, s75, 0x3c00
	v_mbcnt_hi_u32_b32 v209, -1, v2
	v_writelane_b32 v255, s5, 7
	v_cmp_lt_u32_e64 s[4:5], v15, v7
	v_add_u32_e32 v215, v194, v16
	v_add_u32_e32 v216, v194, v17
	v_writelane_b32 v255, s4, 8
	v_add_u32_e32 v221, v14, v8
	v_add_u32_e32 v222, v14, v10
	v_writelane_b32 v255, s5, 9
	v_cmp_gt_u32_e64 s[4:5], v15, v7
	v_or_b32_e32 v15, 19, v12
	v_cmp_gt_u32_e64 s[54:55], v15, v7
	v_writelane_b32 v255, s4, 10
	v_add_u32_e32 v223, v14, v11
	v_add_u32_e32 v224, v14, v3
	v_writelane_b32 v255, s5, 11
	v_cmp_lt_u32_e64 s[4:5], v15, v7
	v_or_b32_e32 v15, 24, v12
	v_cmp_lt_u32_e64 s[56:57], v15, v7
	v_cmp_gt_u32_e64 s[58:59], v15, v7
	v_or_b32_e32 v15, 25, v12
	v_cmp_lt_u32_e64 s[60:61], v15, v7
	v_cmp_gt_u32_e64 s[62:63], v15, v7
	v_or_b32_e32 v15, 26, v12
	v_or_b32_e32 v12, 27, v12
	v_cmp_lt_u32_e64 s[68:69], v12, v7
	v_cmp_gt_u32_e64 s[70:71], v12, v7
	v_lshlrev_b32_e32 v12, 5, v4
	v_and_b32_e32 v12, 0x180, v12
	v_lshl_or_b32 v6, v6, 9, v12
	v_cmp_lt_u32_e64 s[64:65], v15, v7
	v_cmp_gt_u32_e64 s[66:67], v15, v7
	v_add_u32_e32 v7, s75, v13
	v_or_b32_e32 v12, 0x800, v6
	v_xor_b32_e32 v4, v5, v4
	v_writelane_b32 v255, s4, 12
	v_add_u32_e32 v195, v7, v6
	v_add_u32_e32 v197, v12, v7
	v_add_u32_e32 v7, s83, v13
	v_lshlrev_b32_e32 v4, 4, v4
	v_or_b32_e32 v5, 24, v5
	v_writelane_b32 v255, s5, 13
	v_add_u32_e32 v199, v7, v6
	v_add_u32_e32 v201, v7, v12
	v_xor_b32_e32 v6, 16, v193
	v_xor_b32_e32 v7, 32, v193
	v_xor_b32_e32 v12, 48, v193
	v_xor_b32_e32 v13, 64, v193
	v_xor_b32_e32 v15, 0x50, v193
	v_and_b32_e32 v4, 0x70, v4
	v_lshl_add_u32 v19, v5, 7, s75
	v_or_b32_e32 v206, s3, v5
	v_mov_b32_e32 v5, 0x800
	s_add_i32 s4, s22, 0x7f8
	v_add_u32_e32 v196, 64, v195
	v_add_u32_e32 v198, 64, v197
	v_add_u32_e32 v200, 64, v199
	v_add_u32_e32 v202, 64, v201
	v_lshl_or_b32 v207, v9, 4, v5
	v_writelane_b32 v255, s4, 14
	s_add_i32 s22, s75, 0x2000
	v_add_u32_e32 v210, v194, v6
	v_add_u32_e32 v211, v194, v7
	v_add_u32_e32 v212, v194, v12
	v_add_u32_e32 v213, v194, v13
	v_add_u32_e32 v214, v194, v15
	v_add_u32_e32 v217, v18, v4
	v_add_u32_e32 v218, v20, v4
	v_add_u32_e32 v219, v21, v4
	v_add_u32_e32 v220, v19, v4
	v_mov_b32_e32 v226, 0xff800000
	s_mov_b32 s53, 0
	v_bfe_u32 v246, v0, 3, 3
	v_and_b32_e32 v251, 7, v0
	v_xor_b32_e32 v247, v251, v246
	v_lshlrev_b32_e32 v247, 4, v247
	v_add_u32_e32 v247, 0x800, v247
	v_lshlrev_b32_e32 v248, 4, v251
	v_add_u32_e32 v248, 0x1000, v248
	v_add_u32_e32 v249, s3, v246
	v_add_u32_e32 v249, 32, v249
	s_cmp_eq_u32 s3, 0
	s_cselect_b32 s4, 0, 0x80
	s_add_i32 s4, s4, s3
	v_add_u32_e32 v250, s4, v246
	s_branch .LBB0_431

.LBB0_461:
.LBB0_462:
.LBB0_464:
.LBB0_465:
	v_lshlrev_b32_e32 v82, s48, v1
	v_add_u32_e32 v183, s80, v82
	v_mov_b64_e32 v[82:83], s[84:85]
	v_mad_i64_i32 v[82:83], s[4:5], v183, s21, v[82:83]
	s_lshl_b32 s90, s47, 1
	v_lshl_add_u64 v[82:83], v[82:83], 0, s[90:91]
	v_mov_b32_e32 v187, v179
	v_lshl_add_u64 v[82:83], v[82:83], 0, v[186:187]
	global_load_dwordx4 v[162:165], v[82:83], off
	global_load_dwordx4 v[166:169], v[82:83], off offset:32
	global_load_dwordx4 v[170:173], v[82:83], off offset:64
	global_load_dwordx4 v[174:177], v[82:83], off offset:96
	s_lshl_b32 s4, 0xffffff80, s48
	s_lshl_b32 s47, 1, s48
	s_add_i32 s48, s80, s4
	v_add_u32_e32 v187, v208, v84
	s_lshl_b32 s4, s40, 7
	v_add_u32_e32 v82, s4, v247
	s_lshl_b32 s5, s47, 3
	v_mul_u32_u24_e32 v83, s47, v249
	v_add_u32_e32 v83, s48, v83
	v_max_i32_e32 v85, 0, v83
	s_add_u32 m0, s24, 0x8000
	v_mad_u32_u24 v86, v85, s21, v82
	global_load_lds_dwordx4 v86, s[84:85]
	v_add_u32_e32 v83, s5, v83
	v_max_i32_e32 v85, 0, v83
	s_add_u32 m0, s24, 0x8400
	v_mad_u32_u24 v86, v85, s21, v82
	global_load_lds_dwordx4 v86, s[84:85]
	v_add_u32_e32 v83, s5, v83
	v_max_i32_e32 v85, 0, v83
	s_add_u32 m0, s24, 0x8800
	v_mad_u32_u24 v86, v85, s21, v82
	global_load_lds_dwordx4 v86, s[84:85]
	v_add_u32_e32 v83, s5, v83
	v_max_i32_e32 v85, 0, v83
	s_add_u32 m0, s24, 0x8c00
	v_mad_u32_u24 v86, v85, s21, v82
	global_load_lds_dwordx4 v86, s[84:85]
	v_mul_u32_u24_e32 v83, s47, v250
	v_add_u32_e32 v83, s48, v83
	v_max_i32_e32 v85, 0, v83
	s_add_u32 m0, s26, 0x8000
	v_mad_u32_u24 v86, v85, s21, v82
	global_load_lds_dwordx4 v86, s[84:85]
	v_add_u32_e32 v83, s5, v83
	v_max_i32_e32 v85, 0, v83
	s_add_u32 m0, s26, 0x8400
	v_mad_u32_u24 v86, v85, s21, v82
	global_load_lds_dwordx4 v86, s[84:85]
	v_add_u32_e32 v83, s5, v83
	v_max_i32_e32 v85, 0, v83
	s_add_u32 m0, s26, 0x8800
	v_mad_u32_u24 v86, v85, s21, v82
	global_load_lds_dwordx4 v86, s[84:85]
	v_add_u32_e32 v83, s5, v83
	v_max_i32_e32 v85, 0, v83
	s_add_u32 m0, s26, 0x8c00
	v_mad_u32_u24 v86, v85, s21, v82
	global_load_lds_dwordx4 v86, s[84:85]

.LBB0_471:
	v_cndmask_b32_e64 v70, v81, v226, s[78:79]
	v_max3_f32 v33, v18, v97, v20
	v_max3_f32 v33, v33, v19, v22
	v_max3_f32 v33, v33, v21, v24
	v_max3_f32 v33, v33, v23, v26
	v_max3_f32 v33, v33, v25, v28
	v_max3_f32 v33, v33, v27, v31
	v_max3_f32 v33, v33, v29, v30
	v_max3_f32 v33, v33, v32, v3
	v_max3_f32 v33, v33, v2, v5
	v_max3_f32 v33, v33, v4, v7
	v_max3_f32 v33, v33, v6, v9
	v_max3_f32 v33, v33, v8, v11
	v_max3_f32 v33, v33, v10, v13
	v_max3_f32 v33, v33, v12, v15
	v_max3_f32 v33, v33, v14, v17
	v_max3_f32 v33, v33, v16, v35
	v_max3_f32 v33, v33, v34, v37
	v_max3_f32 v33, v33, v36, v39
	v_max3_f32 v33, v33, v38, v41
	v_max3_f32 v33, v33, v40, v43
	v_max3_f32 v33, v33, v42, v45
	v_max3_f32 v33, v33, v44, v47
	v_max3_f32 v33, v33, v46, v49
	v_max3_f32 v33, v33, v48, v51
	v_max3_f32 v33, v33, v50, v53
	v_max3_f32 v33, v33, v52, v55
	v_max3_f32 v33, v33, v54, v57
	v_max3_f32 v33, v33, v56, v59
	v_max3_f32 v33, v33, v58, v61
	v_max3_f32 v33, v33, v60, v63
	v_max3_f32 v33, v33, v62, v65
	v_max3_f32 v33, v33, v64, v83
	v_max3_f32 v33, v33, v82, v85
	v_max3_f32 v33, v33, v84, v87
	v_max3_f32 v33, v33, v86, v89
	v_max3_f32 v33, v33, v88, v91
	v_max3_f32 v33, v33, v90, v93
	v_max3_f32 v33, v33, v92, v95
	v_max3_f32 v33, v33, v94, v70
	v_max_f32_e32 v33, v33, v96
	v_and_b32_e32 v67, 64, v209
	v_xor_b32_e32 v66, 32, v209
	v_add_u32_e32 v67, 64, v67
	v_cmp_lt_i32_e32 vcc, v66, v67
	s_nop 1
	v_cndmask_b32_e32 v66, v209, v66, vcc
	v_lshlrev_b32_e32 v118, 2, v66
	ds_bpermute_b32 v66, v118, v33
	s_waitcnt lgkmcnt(0)
	v_max_f32_e32 v66, v33, v66
	v_pk_add_f32 v[2:3], v[2:3], v[66:67] op_sel_hi:[1,0] neg_lo:[0,1] neg_hi:[0,1]
	v_pk_add_f32 v[4:5], v[4:5], v[66:67] op_sel_hi:[1,0] neg_lo:[0,1] neg_hi:[0,1]
	v_pk_add_f32 v[6:7], v[6:7], v[66:67] op_sel_hi:[1,0] neg_lo:[0,1] neg_hi:[0,1]
	v_pk_add_f32 v[8:9], v[8:9], v[66:67] op_sel_hi:[1,0] neg_lo:[0,1] neg_hi:[0,1]
	v_pk_add_f32 v[10:11], v[10:11], v[66:67] op_sel_hi:[1,0] neg_lo:[0,1] neg_hi:[0,1]
	v_pk_add_f32 v[12:13], v[12:13], v[66:67] op_sel_hi:[1,0] neg_lo:[0,1] neg_hi:[0,1]
	v_pk_add_f32 v[14:15], v[14:15], v[66:67] op_sel_hi:[1,0] neg_lo:[0,1] neg_hi:[0,1]
	v_pk_add_f32 v[16:17], v[16:17], v[66:67] op_sel_hi:[1,0] neg_lo:[0,1] neg_hi:[0,1]
	v_pk_add_f32 v[18:19], v[18:19], v[66:67] op_sel_hi:[1,0] neg_lo:[0,1] neg_hi:[0,1]
	v_pk_add_f32 v[20:21], v[20:21], v[66:67] op_sel_hi:[1,0] neg_lo:[0,1] neg_hi:[0,1]
	v_pk_add_f32 v[22:23], v[22:23], v[66:67] op_sel_hi:[1,0] neg_lo:[0,1] neg_hi:[0,1]
	v_pk_add_f32 v[24:25], v[24:25], v[66:67] op_sel_hi:[1,0] neg_lo:[0,1] neg_hi:[0,1]
	v_pk_add_f32 v[26:27], v[26:27], v[66:67] op_sel_hi:[1,0] neg_lo:[0,1] neg_hi:[0,1]
	v_pk_add_f32 v[28:29], v[28:29], v[66:67] op_sel_hi:[1,0] neg_lo:[0,1] neg_hi:[0,1]
	v_pk_add_f32 v[30:31], v[30:31], v[66:67] op_sel_hi:[1,0] neg_lo:[0,1] neg_hi:[0,1]
	v_pk_add_f32 v[34:35], v[34:35], v[66:67] op_sel_hi:[1,0] neg_lo:[0,1] neg_hi:[0,1]
	v_pk_add_f32 v[36:37], v[36:37], v[66:67] op_sel_hi:[1,0] neg_lo:[0,1] neg_hi:[0,1]
	v_pk_add_f32 v[38:39], v[38:39], v[66:67] op_sel_hi:[1,0] neg_lo:[0,1] neg_hi:[0,1]
	v_pk_add_f32 v[40:41], v[40:41], v[66:67] op_sel_hi:[1,0] neg_lo:[0,1] neg_hi:[0,1]
	v_pk_add_f32 v[42:43], v[42:43], v[66:67] op_sel_hi:[1,0] neg_lo:[0,1] neg_hi:[0,1]
	v_pk_add_f32 v[44:45], v[44:45], v[66:67] op_sel_hi:[1,0] neg_lo:[0,1] neg_hi:[0,1]
	v_pk_add_f32 v[46:47], v[46:47], v[66:67] op_sel_hi:[1,0] neg_lo:[0,1] neg_hi:[0,1]
	v_pk_add_f32 v[48:49], v[48:49], v[66:67] op_sel_hi:[1,0] neg_lo:[0,1] neg_hi:[0,1]
	v_pk_add_f32 v[50:51], v[50:51], v[66:67] op_sel_hi:[1,0] neg_lo:[0,1] neg_hi:[0,1]
	v_pk_add_f32 v[52:53], v[52:53], v[66:67] op_sel_hi:[1,0] neg_lo:[0,1] neg_hi:[0,1]
	v_pk_add_f32 v[54:55], v[54:55], v[66:67] op_sel_hi:[1,0] neg_lo:[0,1] neg_hi:[0,1]
	v_pk_add_f32 v[56:57], v[56:57], v[66:67] op_sel_hi:[1,0] neg_lo:[0,1] neg_hi:[0,1]
	v_pk_add_f32 v[58:59], v[58:59], v[66:67] op_sel_hi:[1,0] neg_lo:[0,1] neg_hi:[0,1]
	v_pk_add_f32 v[60:61], v[60:61], v[66:67] op_sel_hi:[1,0] neg_lo:[0,1] neg_hi:[0,1]
	v_pk_add_f32 v[62:63], v[62:63], v[66:67] op_sel_hi:[1,0] neg_lo:[0,1] neg_hi:[0,1]
	v_pk_add_f32 v[64:65], v[64:65], v[66:67] op_sel_hi:[1,0] neg_lo:[0,1] neg_hi:[0,1]
	v_pk_add_f32 v[82:83], v[82:83], v[66:67] op_sel_hi:[1,0] neg_lo:[0,1] neg_hi:[0,1]
	v_pk_add_f32 v[84:85], v[84:85], v[66:67] op_sel_hi:[1,0] neg_lo:[0,1] neg_hi:[0,1]
	v_pk_add_f32 v[86:87], v[86:87], v[66:67] op_sel_hi:[1,0] neg_lo:[0,1] neg_hi:[0,1]
	v_pk_add_f32 v[88:89], v[88:89], v[66:67] op_sel_hi:[1,0] neg_lo:[0,1] neg_hi:[0,1]
	v_pk_add_f32 v[90:91], v[90:91], v[66:67] op_sel_hi:[1,0] neg_lo:[0,1] neg_hi:[0,1]
	v_pk_add_f32 v[92:93], v[92:93], v[66:67] op_sel_hi:[1,0] neg_lo:[0,1] neg_hi:[0,1]
	v_pk_add_f32 v[94:95], v[94:95], v[66:67] op_sel_hi:[1,0] neg_lo:[0,1] neg_hi:[0,1]
	v_pk_add_f32 v[96:97], v[96:97], v[66:67] op_sel_hi:[1,0] neg_lo:[0,1] neg_hi:[0,1]
	v_sub_f32_e32 v32, v32, v66
	v_sub_f32_e32 v70, v70, v66
	v_exp_f32_e32 v33, v97
	v_exp_f32_e32 v18, v18
	v_exp_f32_e32 v19, v19
	v_exp_f32_e32 v20, v20
	v_mov_b32_e32 v244, 0
	v_mov_b32_e32 v245, 0
	v_add_f32_e32 v244, v33, v244
	v_exp_f32_e32 v21, v21
	v_exp_f32_e32 v22, v22
	v_pk_add_f32 v[244:245], v[18:19], v[244:245]
	v_exp_f32_e32 v23, v23
	v_exp_f32_e32 v24, v24
	v_pk_add_f32 v[244:245], v[20:21], v[244:245]
	v_exp_f32_e32 v119, v25
	v_exp_f32_e32 v120, v26
	v_pk_add_f32 v[244:245], v[22:23], v[244:245]
	v_exp_f32_e32 v121, v27
	v_add_f32_e32 v244, v24, v244
	v_exp_f32_e32 v122, v28
	v_add_f32_e32 v244, v119, v244
	v_exp_f32_e32 v123, v29
	v_exp_f32_e32 v124, v31
	v_pk_add_f32 v[244:245], v[120:121], v[244:245]
	v_exp_f32_e32 v125, v32
	v_exp_f32_e32 v126, v30
	v_pk_add_f32 v[244:245], v[122:123], v[244:245]
	v_exp_f32_e32 v103, v2
	v_exp_f32_e32 v106, v3
	v_pk_add_f32 v[244:245], v[124:125], v[244:245]
	v_exp_f32_e32 v107, v4
	v_add_f32_e32 v244, v126, v244
	v_exp_f32_e32 v110, v5
	v_exp_f32_e32 v111, v6
	v_exp_f32_e32 v114, v7
	v_pk_add_f32 v[244:245], v[106:107], v[244:245]
	v_exp_f32_e32 v115, v8
	v_exp_f32_e32 v117, v9
	v_pk_add_f32 v[244:245], v[110:111], v[244:245]
	v_exp_f32_e32 v102, v10
	v_exp_f32_e32 v104, v11
	v_pk_add_f32 v[244:245], v[114:115], v[244:245]
	v_exp_f32_e32 v105, v12
	v_exp_f32_e32 v108, v13
	v_pk_add_f32 v[244:245], v[102:103], v[244:245]
	v_exp_f32_e32 v109, v14
	v_exp_f32_e32 v112, v15
	v_pk_add_f32 v[244:245], v[104:105], v[244:245]
	v_exp_f32_e32 v113, v16
	v_exp_f32_e32 v116, v17
	v_pk_add_f32 v[244:245], v[108:109], v[244:245]
	v_exp_f32_e32 v72, v34
	v_exp_f32_e32 v75, v35
	v_pk_add_f32 v[244:245], v[112:113], v[244:245]
	v_exp_f32_e32 v76, v36
	v_pk_add_f32 v[244:245], v[116:117], v[244:245]
	v_exp_f32_e32 v79, v37
	v_exp_f32_e32 v80, v38
	v_exp_f32_e32 v98, v39
	v_exp_f32_e32 v99, v40
	v_exp_f32_e32 v101, v41
	v_exp_f32_e32 v71, v42
	v_exp_f32_e32 v73, v43
	v_pk_add_f32 v[244:245], v[98:99], v[244:245]
	v_exp_f32_e32 v74, v44
	v_exp_f32_e32 v77, v45
	v_exp_f32_e32 v78, v46
	v_pk_add_f32 v[244:245], v[72:73], v[244:245]
	v_exp_f32_e32 v81, v47
	v_pk_add_f32 v[244:245], v[74:75], v[244:245]
	v_exp_f32_e32 v97, v48
	v_pk_add_f32 v[244:245], v[76:77], v[244:245]
	v_exp_f32_e32 v100, v49
	v_pk_add_f32 v[244:245], v[78:79], v[244:245]
	v_exp_f32_e32 v41, v50
	v_pk_add_f32 v[244:245], v[80:81], v[244:245]
	v_exp_f32_e32 v46, v51
	v_add_f32_e32 v244, v97, v244
	v_exp_f32_e32 v47, v52
	v_pk_add_f32 v[244:245], v[100:101], v[244:245]
	v_exp_f32_e32 v53, v53
	v_exp_f32_e32 v54, v54
	v_exp_f32_e32 v67, v55
	v_pk_add_f32 v[244:245], v[46:47], v[244:245]
	v_exp_f32_e32 v68, v56
	v_exp_f32_e32 v69, v57
	v_exp_f32_e32 v38, v58
	v_add_f32_e32 v244, v67, v244
	v_exp_f32_e32 v44, v59
	v_exp_f32_e32 v45, v60
	v_pk_add_f32 v[244:245], v[68:69], v[244:245]
	v_exp_f32_e32 v51, v61
	v_exp_f32_e32 v52, v62
	v_exp_f32_e32 v57, v63
	v_pk_add_f32 v[244:245], v[44:45], v[244:245]
	v_exp_f32_e32 v58, v64
	v_exp_f32_e32 v62, v65
	v_pk_add_f32 v[244:245], v[52:53], v[244:245]
	v_exp_f32_e32 v37, v82
	v_exp_f32_e32 v42, v83
	v_add_f32_e32 v244, v58, v244
	v_exp_f32_e32 v43, v84
	v_exp_f32_e32 v49, v85
	v_exp_f32_e32 v50, v86
	v_exp_f32_e32 v55, v87
	v_pk_add_f32 v[244:245], v[42:43], v[244:245]
	v_exp_f32_e32 v56, v88
	v_exp_f32_e32 v61, v89
	v_pk_add_f32 v[244:245], v[50:51], v[244:245]
	v_exp_f32_e32 v36, v90
	v_pk_add_f32 v[244:245], v[54:55], v[244:245]
	v_exp_f32_e32 v39, v91
	v_pk_add_f32 v[244:245], v[56:57], v[244:245]
	v_exp_f32_e32 v40, v92
	v_add_f32_e32 v244, v61, v244
	v_pk_add_f32 v[244:245], v[36:37], v[244:245]
	v_pk_add_f32 v[244:245], v[38:39], v[244:245]
	v_pk_add_f32 v[244:245], v[40:41], v[244:245]
	v_exp_f32_e32 v48, v93
	v_cvt_pk_bf16_f32 v2, v33, v18
	v_cvt_pk_bf16_f32 v3, v19, v20
	v_cvt_pk_bf16_f32 v4, v21, v22
	v_cvt_pk_bf16_f32 v5, v23, v24
	s_bitcmp1_b32 s96, 0
	s_cbranch_scc1 .Latt_b3m
	s_waitcnt vmcnt(0)
.Latt_b3m:
	s_waitcnt vmcnt(12)
	s_barrier
	ds_read_b64_tr_b16 v[228:229], v195
	ds_read_b64_tr_b16 v[230:231], v195 offset:1024
	ds_read_b64_tr_b16 v[232:233], v196
	ds_read_b64_tr_b16 v[234:235], v196 offset:1024
	s_waitcnt lgkmcnt(0)
	ds_read_b64_tr_b16 v[236:237], v197
	ds_read_b64_tr_b16 v[238:239], v197 offset:1024
	ds_read_b64_tr_b16 v[240:241], v198
	ds_read_b64_tr_b16 v[242:243], v198 offset:1024
	s_nop 0
	v_pk_add_f32 v[244:245], v[48:49], v[244:245]
	v_mfma_f32_32x32x16_bf16 v[18:33], v[228:231], v[2:5], 0
	v_exp_f32_e32 v63, v94
	v_exp_f32_e32 v65, v95
	v_exp_f32_e32 v64, v96
	v_mfma_f32_32x32x16_bf16 v[2:17], v[232:235], v[2:5], 0
	v_exp_f32_e32 v70, v70
	v_pk_add_f32 v[244:245], v[62:63], v[244:245]
	v_cvt_pk_bf16_f32 v82, v119, v120
	v_cvt_pk_bf16_f32 v83, v121, v122
	v_cvt_pk_bf16_f32 v84, v123, v124
	v_cvt_pk_bf16_f32 v85, v125, v126
	s_waitcnt lgkmcnt(0)
	ds_read_b64_tr_b16 v[228:229], v199
	ds_read_b64_tr_b16 v[230:231], v199 offset:1024
	ds_read_b64_tr_b16 v[232:233], v200
	ds_read_b64_tr_b16 v[234:235], v200 offset:1024
	v_mfma_f32_32x32x16_bf16 v[18:33], v[236:239], v[82:85], v[18:33]
	v_pk_add_f32 v[244:245], v[64:65], v[244:245]
	v_pk_add_f32 v[244:245], v[70:71], v[244:245]
	v_add_f32_e32 v59, v244, v245
	ds_bpermute_b32 v60, v118, v59
	v_mfma_f32_32x32x16_bf16 v[2:17], v[240:243], v[82:85], v[2:17]

.LBB0_485:
	s_waitcnt vmcnt(0)
	s_barrier
	s_waitcnt lgkmcnt(0)
	v_add_f32_e32 v34, v59, v60
	v_div_scale_f32 v35, s[4:5], v34, v34, 1.0
	v_rcp_f32_e32 v36, v35
	v_div_scale_f32 v37, vcc, 1.0, v34, 1.0
	s_ashr_i32 s87, s86, 31
	v_fma_f32 v38, -v35, v36, 1.0
	v_fmac_f32_e32 v36, v38, v36
	v_mul_f32_e32 v38, v37, v36
	v_fma_f32 v39, -v35, v38, v37
	v_fmac_f32_e32 v38, v39, v36
	v_fma_f32 v35, -v35, v38, v37
	v_div_fmas_f32 v35, v35, v36, v38
	v_div_fixup_f32 v35, v35, v34, 1.0
	v_pk_mul_f32 v[18:19], v[18:19], v[34:35] op_sel:[0,1] op_sel_hi:[1,1]
	v_pk_mul_f32 v[20:21], v[20:21], v[34:35] op_sel:[0,1] op_sel_hi:[1,1]
	v_pk_mul_f32 v[22:23], v[22:23], v[34:35] op_sel:[0,1] op_sel_hi:[1,1]
	v_pk_mul_f32 v[24:25], v[24:25], v[34:35] op_sel:[0,1] op_sel_hi:[1,1]
	v_pk_mul_f32 v[26:27], v[26:27], v[34:35] op_sel:[0,1] op_sel_hi:[1,1]
	v_pk_mul_f32 v[28:29], v[28:29], v[34:35] op_sel:[0,1] op_sel_hi:[1,1]
	v_pk_mul_f32 v[30:31], v[30:31], v[34:35] op_sel:[0,1] op_sel_hi:[1,1]
	v_pk_mul_f32 v[32:33], v[32:33], v[34:35] op_sel:[0,1] op_sel_hi:[1,1]
	v_pk_mul_f32 v[2:3], v[2:3], v[34:35] op_sel:[0,1] op_sel_hi:[1,1]
	v_pk_mul_f32 v[4:5], v[4:5], v[34:35] op_sel:[0,1] op_sel_hi:[1,1]
	v_pk_mul_f32 v[6:7], v[6:7], v[34:35] op_sel:[0,1] op_sel_hi:[1,1]
	v_pk_mul_f32 v[8:9], v[8:9], v[34:35] op_sel:[0,1] op_sel_hi:[1,1]
	v_pk_mul_f32 v[10:11], v[10:11], v[34:35] op_sel:[0,1] op_sel_hi:[1,1]
	v_pk_mul_f32 v[12:13], v[12:13], v[34:35] op_sel:[0,1] op_sel_hi:[1,1]
	v_pk_mul_f32 v[14:15], v[14:15], v[34:35] op_sel:[0,1] op_sel_hi:[1,1]
	v_pk_mul_f32 v[16:17], v[16:17], v[34:35] op_sel:[0,1] op_sel_hi:[1,1]
	v_cvt_pk_bf16_f32 v18, v18, v19
	v_cvt_pk_bf16_f32 v19, v20, v21
	v_add_u32_e32 v20, v194, v193
	ds_write_b64 v20, v[18:19] offset:4096
	v_cvt_pk_bf16_f32 v18, v22, v23
	v_cvt_pk_bf16_f32 v19, v24, v25
	ds_write_b64 v210, v[18:19] offset:4096
	v_cvt_pk_bf16_f32 v18, v26, v27
	v_cvt_pk_bf16_f32 v19, v28, v29
	ds_write_b64 v211, v[18:19] offset:4096
	v_cvt_pk_bf16_f32 v18, v30, v31
	v_cvt_pk_bf16_f32 v19, v32, v33
	ds_write_b64 v212, v[18:19] offset:4096
	v_cvt_pk_bf16_f32 v2, v2, v3
	v_cvt_pk_bf16_f32 v3, v4, v5
	ds_write_b64 v213, v[2:3] offset:4096
	v_cvt_pk_bf16_f32 v2, v6, v7
	v_cvt_pk_bf16_f32 v3, v8, v9
	ds_write_b64 v214, v[2:3] offset:4096
	v_cvt_pk_bf16_f32 v2, v10, v11
	v_cvt_pk_bf16_f32 v3, v12, v13
	ds_write_b64 v215, v[2:3] offset:4096
	v_cvt_pk_bf16_f32 v2, v14, v15
	v_cvt_pk_bf16_f32 v3, v16, v17
	ds_write_b64 v216, v[2:3] offset:4096
	s_lshl_b64 s[4:5], s[86:87], 14
	s_ashr_i32 s43, s42, 31
	s_add_u32 s4, s4, s42
	ds_read_b128 v[2:5], v217 offset:4096
	v_mul_lo_u32 v6, s81, v203
	s_addc_u32 s5, s5, s43
	v_ashrrev_i32_e32 v7, 31, v6
	s_lshl_b32 s90, s37, 1
	v_lshl_add_u64 v[6:7], s[4:5], 0, v[6:7]
	v_lshl_add_u64 v[10:11], v[184:185], 0, s[90:91]
	v_lshlrev_b64 v[6:7], 11, v[6:7]
	v_lshl_add_u64 v[12:13], v[10:11], 0, v[6:7]
	ds_read_b128 v[6:9], v218 offset:4096
	s_waitcnt lgkmcnt(0)
	global_store_dwordx4 v[12:13], v[2:5], off nt
	s_nop 1
	v_mul_lo_u32 v2, s81, v204
	v_ashrrev_i32_e32 v3, 31, v2
	v_lshl_add_u64 v[2:3], s[4:5], 0, v[2:3]
	v_lshlrev_b64 v[2:3], 11, v[2:3]
	v_lshl_add_u64 v[2:3], v[10:11], 0, v[2:3]
	global_store_dwordx4 v[2:3], v[6:9], off nt
	ds_read_b128 v[2:5], v219 offset:4096
	s_nop 0
	v_mul_lo_u32 v6, s81, v205
	v_ashrrev_i32_e32 v7, 31, v6
	v_lshl_add_u64 v[6:7], s[4:5], 0, v[6:7]
	v_lshlrev_b64 v[6:7], 11, v[6:7]
	v_lshl_add_u64 v[12:13], v[10:11], 0, v[6:7]
	ds_read_b128 v[6:9], v220 offset:4096
	s_waitcnt lgkmcnt(0)
	global_store_dwordx4 v[12:13], v[2:5], off nt
	s_nop 1
	v_mul_lo_u32 v2, s81, v206
	v_ashrrev_i32_e32 v3, 31, v2
	v_lshl_add_u64 v[2:3], s[4:5], 0, v[2:3]
	v_lshlrev_b64 v[2:3], 11, v[2:3]
	v_lshl_add_u64 v[2:3], v[10:11], 0, v[2:3]
	global_store_dwordx4 v[2:3], v[6:9], off nt
	s_and_saveexec_b64 s[4:5], s[6:7]
	s_cbranch_execz .LBB0_487
	v_log_f32_e32 v2, v34
	s_lshl_b64 s[44:45], s[86:87], 20
	v_readlane_b32 s37, v254, 17
	v_ashrrev_i32_e32 v181, 31, v180
	v_add_f32_e32 v2, v66, v2
	s_add_u32 s44, s37, s44
	v_readlane_b32 s37, v254, 18
	v_mul_f32_e32 v4, 0x3f317218, v2
	s_addc_u32 s45, s37, s45
	v_lshlrev_b64 v[2:3], 6, v[180:181]
	s_mov_b32 s89, s91
	v_lshl_add_u64 v[2:3], s[44:45], 0, v[2:3]
	v_lshl_add_u64 v[2:3], s[88:89], 2, v[2:3]
	global_store_dword v[2:3], v4, off
.LBB0_487:
	s_or_b64 exec, exec, s[4:5]
	s_waitcnt lgkmcnt(0)
	s_and_b64 vcc, exec, s[72:73]
	s_cbranch_vccnz .LBB0_430
	v_mov_b64_e32 v[146:147], v[174:175]
	v_mov_b64_e32 v[150:151], v[170:171]
	v_mov_b64_e32 v[154:155], v[166:167]
	v_mov_b64_e32 v[158:159], v[162:163]
	v_mov_b64_e32 v[148:149], v[176:177]
	v_mov_b64_e32 v[152:153], v[172:173]
	v_mov_b64_e32 v[156:157], v[168:169]
	v_mov_b64_e32 v[160:161], v[164:165]
	v_mov_b32_e32 v182, v187
	v_mov_b32_e32 v178, v190
	v_mov_b32_e32 v180, v183
	s_mov_b32 s82, s48
	s_mov_b32 s42, s80
	s_mov_b32 s33, s41
	s_mov_b32 s81, s47
	s_mov_b32 s88, s40
	s_mov_b32 s86, s39
	s_lshl_b32 s4, s88, 7
	v_add_u32_e32 v2, s4, v248
	s_lshl_b32 s5, s81, 3
	v_mul_u32_u24_e32 v3, s81, v249
	v_add_u32_e32 v3, s82, v3
	v_max_i32_e32 v4, 0, v3
	s_mov_b32 m0, s24
	v_mad_u32_u24 v5, v4, s21, v2
	global_load_lds_dwordx4 v5, s[84:85]
	v_add_u32_e32 v3, s5, v3
	v_max_i32_e32 v4, 0, v3
	s_add_u32 m0, s24, 0x400
	v_mad_u32_u24 v5, v4, s21, v2
	global_load_lds_dwordx4 v5, s[84:85]
	v_add_u32_e32 v3, s5, v3
	v_max_i32_e32 v4, 0, v3
	s_add_u32 m0, s24, 0x800
	v_mad_u32_u24 v5, v4, s21, v2
	global_load_lds_dwordx4 v5, s[84:85]
	v_add_u32_e32 v3, s5, v3
	v_max_i32_e32 v4, 0, v3
	s_add_u32 m0, s24, 0xc00
	v_mad_u32_u24 v5, v4, s21, v2
	global_load_lds_dwordx4 v5, s[84:85]
	v_mul_u32_u24_e32 v3, s81, v250
	v_add_u32_e32 v3, s82, v3
	v_max_i32_e32 v4, 0, v3
	s_mov_b32 m0, s26
	v_mad_u32_u24 v5, v4, s21, v2
	global_load_lds_dwordx4 v5, s[84:85]
	v_add_u32_e32 v3, s5, v3
	v_max_i32_e32 v4, 0, v3
	s_add_u32 m0, s26, 0x400
	v_mad_u32_u24 v5, v4, s21, v2
	global_load_lds_dwordx4 v5, s[84:85]
	v_add_u32_e32 v3, s5, v3
	v_max_i32_e32 v4, 0, v3
	s_add_u32 m0, s26, 0x800
	v_mad_u32_u24 v5, v4, s21, v2
	global_load_lds_dwordx4 v5, s[84:85]
	v_add_u32_e32 v3, s5, v3
	v_max_i32_e32 v4, 0, v3
	s_add_u32 m0, s26, 0xc00
	v_mad_u32_u24 v5, v4, s21, v2
	global_load_lds_dwordx4 v5, s[84:85]
	s_branch .LBB0_430
